# speedup vs baseline: 1.1450x; 1.0084x over previous
.LBB0_21:
	v_exp_f32_e64 v156, -|v154|
	v_max_f32 v157, 0, v154
	v_add_f32 v156, 1.0, v156
	v_log_f32 v156, v156
	s_nop 0
	v_fma_mixlo_f16 v155, v156, 1.0, v157
	ds_write_b16 v148, v155
	v_mov_b32_e32 v192, v106
	v_mov_b32_e32 v193, v110
	v_mul_f32 v182, -2.0, v153
	s_nop 6
	ds_read_b128 v[208:211], v139
	s_waitcnt lgkmcnt(1)
	s_barrier
	ds_read_b128 v[212:215], v140
	s_waitcnt lgkmcnt(1)
	v_smfmac_f32_16x16x64_f16 v[192:195], v[208:211], v[6:13], v191
	ds_read_b128 v[216:219], v141
	s_waitcnt lgkmcnt(1)
	v_smfmac_f32_16x16x64_f16 v[192:195], v[212:215], v[14:21], v191
	ds_read_b128 v[220:223], v142
	s_waitcnt lgkmcnt(1)
	v_smfmac_f32_16x16x64_f16 v[192:195], v[216:219], v[26:33], v191
	s_waitcnt lgkmcnt(0)
	v_smfmac_f32_16x16x64_f16 v[192:195], v[220:223], v[34:41], v191
	s_nop 7
	v_cndmask_b32_e64 v154, v192, v193, s[0:1]
	v_exp_f32_e64 v156, -|v154|
	v_max_f32 v157, 0, v154
	v_add_f32 v156, 1.0, v156
	v_log_f32 v156, v156
	s_nop 0
	v_fma_mixlo_f16 v155, v156, 1.0, v157
	ds_write_b16 v149, v155
	v_mov_b32_e32 v200, v114
	v_mov_b32_e32 v201, v118
	v_mov_b32_e32 v204, v122
	v_mov_b32_e32 v205, v126
	s_nop 2
	ds_read_b128 v[208:211], v143
	s_waitcnt lgkmcnt(1)
	s_barrier
	ds_read_b128 v[212:215], v144
	s_waitcnt lgkmcnt(1)
	v_smfmac_f32_16x16x64_f16 v[200:203], v[208:211], v[42:49], v191
	ds_read_b128 v[216:219], v145
	v_smfmac_f32_16x16x64_f16 v[204:207], v[208:211], v[74:81], v191
	ds_read_b128 v[220:223], v146
	s_waitcnt lgkmcnt(2)
	v_smfmac_f32_16x16x64_f16 v[200:203], v[212:215], v[50:57], v191
	v_smfmac_f32_16x16x64_f16 v[204:207], v[212:215], v[82:89], v191
	s_waitcnt lgkmcnt(1)
	v_smfmac_f32_16x16x64_f16 v[200:203], v[216:219], v[58:65], v191
	v_smfmac_f32_16x16x64_f16 v[204:207], v[216:219], v[90:97], v191
	s_waitcnt lgkmcnt(0)
	v_smfmac_f32_16x16x64_f16 v[200:203], v[220:223], v[66:73], v191
	v_smfmac_f32_16x16x64_f16 v[204:207], v[220:223], v[98:105], v191
	s_nop 6
	v_cndmask_b32_e64 v170, v201, v200, s[6:7]
	v_cndmask_b32_e64 v170, v170, v204, s[0:1]
	v_cndmask_b32_e64 v170, v170, v205, s[4:5]
	v_exp_f32_e32 v170, v170
	s_nop 0
	v_add_f32_e32 v170, 1.0, v170
	v_rcp_f32_e32 v170, v170
	s_nop 0
	v_fmac_f32_e32 v153, v170, v182
	s_nop 1
	v_add_f32_dpp v153, v153, v153 quad_perm:[1,0,3,2] row_mask:0xf bank_mask:0xf bound_ctrl:1
	s_nop 1
	v_add_f32_dpp v153, v153, v153 quad_perm:[2,3,0,1] row_mask:0xf bank_mask:0xf bound_ctrl:1
	s_nop 1
	v_add_f32_dpp v153, v153, v153 row_half_mirror row_mask:0xf bank_mask:0xf bound_ctrl:1
	v_cvt_f16_f32_e32 v170, v153
	ds_write_b16 v150, v170
	s_waitcnt lgkmcnt(0)
	s_barrier
	ds_read_b128 v[154:157], v147
	s_waitcnt lgkmcnt(0)
	v_smfmac_f32_16x16x64_f16 v[130:133], v[154:157], v[248:255], v191
	s_nop 2
	v_add_u32_e32 v134, s3, v151
	ds_read_b32 v135, v134
	s_nop 2
	v_cndmask_b32_e64 v136, v130, v131, s[0:1]
	v_exp_f32_e64 v158, -|v136|
	v_max_f32 v159, 0, v136
	v_add_f32 v158, 1.0, v158
	v_log_f32 v158, v158
	s_nop 0
	v_fma_mixlo_f16 v137, v158, 1.0, v159
	ds_write_b16 v148, v137
	v_mov_b32_e32 v192, v106
	v_mov_b32_e32 v193, v110
	v_add_f32_e32 v136, v152, v153
	v_mul_f32 v137, -2.0, v135
	s_nop 6
	ds_read_b128 v[208:211], v139
	s_waitcnt lgkmcnt(1)
	s_barrier
	ds_read_b128 v[212:215], v140
	s_waitcnt lgkmcnt(1)
	v_smfmac_f32_16x16x64_f16 v[192:195], v[208:211], v[6:13], v191
	ds_read_b128 v[216:219], v141
	s_waitcnt lgkmcnt(1)
	v_smfmac_f32_16x16x64_f16 v[192:195], v[212:215], v[14:21], v191
	ds_read_b128 v[220:223], v142
	s_waitcnt lgkmcnt(1)
	v_smfmac_f32_16x16x64_f16 v[192:195], v[216:219], v[26:33], v191
	s_waitcnt lgkmcnt(0)
	v_smfmac_f32_16x16x64_f16 v[192:195], v[220:223], v[34:41], v191
	s_nop 7
	v_cndmask_b32_e64 v152, v192, v193, s[0:1]
	v_exp_f32_e64 v158, -|v152|
	v_max_f32 v159, 0, v152
	v_add_f32 v158, 1.0, v158
	v_log_f32 v158, v158
	s_nop 0
	v_fma_mixlo_f16 v153, v158, 1.0, v159
	ds_write_b16 v149, v153
	v_mov_b32_e32 v200, v114
	v_mov_b32_e32 v201, v118
	v_mov_b32_e32 v204, v122
	v_mov_b32_e32 v205, v126
	s_nop 2
	ds_read_b128 v[208:211], v143
	s_waitcnt lgkmcnt(1)
	s_barrier
	ds_read_b128 v[212:215], v144
	s_waitcnt lgkmcnt(1)
	v_smfmac_f32_16x16x64_f16 v[200:203], v[208:211], v[42:49], v191
	ds_read_b128 v[216:219], v145
	v_smfmac_f32_16x16x64_f16 v[204:207], v[208:211], v[74:81], v191
	ds_read_b128 v[220:223], v146
	s_waitcnt lgkmcnt(2)
	v_smfmac_f32_16x16x64_f16 v[200:203], v[212:215], v[50:57], v191
	v_smfmac_f32_16x16x64_f16 v[204:207], v[212:215], v[82:89], v191
	s_waitcnt lgkmcnt(1)
	v_smfmac_f32_16x16x64_f16 v[200:203], v[216:219], v[58:65], v191
	v_smfmac_f32_16x16x64_f16 v[204:207], v[216:219], v[90:97], v191
	s_waitcnt lgkmcnt(0)
	v_smfmac_f32_16x16x64_f16 v[200:203], v[220:223], v[66:73], v191
	v_smfmac_f32_16x16x64_f16 v[204:207], v[220:223], v[98:105], v191
	s_nop 6
	v_cndmask_b32_e64 v152, v201, v200, s[6:7]
	v_cndmask_b32_e64 v152, v152, v204, s[0:1]
	v_cndmask_b32_e64 v152, v152, v205, s[4:5]
	v_exp_f32_e32 v152, v152
	s_nop 0
	v_add_f32_e32 v152, 1.0, v152
	v_rcp_f32_e32 v152, v152
	s_nop 0
	v_fmac_f32_e32 v135, v152, v137
	s_nop 1
	v_add_f32_dpp v135, v135, v135 quad_perm:[1,0,3,2] row_mask:0xf bank_mask:0xf bound_ctrl:1
	s_nop 1
	v_add_f32_dpp v135, v135, v135 quad_perm:[2,3,0,1] row_mask:0xf bank_mask:0xf bound_ctrl:1
	s_nop 1
	v_add_f32_dpp v135, v135, v135 row_half_mirror row_mask:0xf bank_mask:0xf bound_ctrl:1
	v_cvt_f16_f32_e32 v137, v135
	ds_write_b16 v150, v137
	s_waitcnt lgkmcnt(0)
	s_barrier
	ds_read_b128 v[158:161], v147
	ds_read_b32 v137, v134 offset:32
	v_add_f32_e32 v135, v136, v135
	s_waitcnt lgkmcnt(1)
	v_smfmac_f32_16x16x64_f16 v[130:133], v[158:161], v[248:255], v191
	s_nop 7
	v_cndmask_b32_e64 v156, v130, v131, s[0:1]
	v_exp_f32_e64 v158, -|v156|
	v_max_f32 v159, 0, v156
	v_add_f32 v158, 1.0, v158
	v_log_f32 v158, v158
	s_nop 0
	v_fma_mixlo_f16 v157, v158, 1.0, v159
	ds_write_b16 v148, v157
	v_mov_b32_e32 v192, v106
	v_mov_b32_e32 v193, v110
	v_mul_f32 v136, -2.0, v137
	s_nop 6
	ds_read_b128 v[208:211], v139
	s_waitcnt lgkmcnt(1)
	s_barrier
	ds_read_b128 v[212:215], v140
	s_waitcnt lgkmcnt(1)
	v_smfmac_f32_16x16x64_f16 v[192:195], v[208:211], v[6:13], v191
	ds_read_b128 v[216:219], v141
	s_waitcnt lgkmcnt(1)
	v_smfmac_f32_16x16x64_f16 v[192:195], v[212:215], v[14:21], v191
	ds_read_b128 v[220:223], v142
	s_waitcnt lgkmcnt(1)
	v_smfmac_f32_16x16x64_f16 v[192:195], v[216:219], v[26:33], v191
	s_waitcnt lgkmcnt(0)
	v_smfmac_f32_16x16x64_f16 v[192:195], v[220:223], v[34:41], v191
	s_nop 7
	v_cndmask_b32_e64 v156, v192, v193, s[0:1]
	v_exp_f32_e64 v158, -|v156|
	v_max_f32 v159, 0, v156
	v_add_f32 v158, 1.0, v158
	v_log_f32 v158, v158
	s_nop 0
	v_fma_mixlo_f16 v157, v158, 1.0, v159
	ds_write_b16 v149, v157
	v_mov_b32_e32 v200, v114
	v_mov_b32_e32 v201, v118
	v_mov_b32_e32 v204, v122
	v_mov_b32_e32 v205, v126
	s_nop 2
	ds_read_b128 v[208:211], v143
	s_waitcnt lgkmcnt(1)
	s_barrier
	ds_read_b128 v[212:215], v144
	s_waitcnt lgkmcnt(1)
	v_smfmac_f32_16x16x64_f16 v[200:203], v[208:211], v[42:49], v191
	ds_read_b128 v[216:219], v145
	v_smfmac_f32_16x16x64_f16 v[204:207], v[208:211], v[74:81], v191
	ds_read_b128 v[220:223], v146
	s_waitcnt lgkmcnt(2)
	v_smfmac_f32_16x16x64_f16 v[200:203], v[212:215], v[50:57], v191
	v_smfmac_f32_16x16x64_f16 v[204:207], v[212:215], v[82:89], v191
	s_waitcnt lgkmcnt(1)
	v_smfmac_f32_16x16x64_f16 v[200:203], v[216:219], v[58:65], v191
	v_smfmac_f32_16x16x64_f16 v[204:207], v[216:219], v[90:97], v191
	s_waitcnt lgkmcnt(0)
	v_smfmac_f32_16x16x64_f16 v[200:203], v[220:223], v[66:73], v191
	v_smfmac_f32_16x16x64_f16 v[204:207], v[220:223], v[98:105], v191
	s_nop 6
	v_cndmask_b32_e64 v172, v201, v200, s[6:7]
	v_cndmask_b32_e64 v172, v172, v204, s[0:1]
	v_cndmask_b32_e64 v172, v172, v205, s[4:5]
	v_exp_f32_e32 v172, v172
	s_nop 0
	v_add_f32_e32 v172, 1.0, v172
	v_rcp_f32_e32 v172, v172
	s_nop 0
	v_fmac_f32_e32 v137, v172, v136
	s_nop 1
	v_add_f32_dpp v136, v137, v137 quad_perm:[1,0,3,2] row_mask:0xf bank_mask:0xf bound_ctrl:1
	s_nop 1
	v_add_f32_dpp v136, v136, v136 quad_perm:[2,3,0,1] row_mask:0xf bank_mask:0xf bound_ctrl:1
	s_nop 1
	v_add_f32_dpp v136, v136, v136 row_half_mirror row_mask:0xf bank_mask:0xf bound_ctrl:1
	v_cvt_f16_f32_e32 v137, v136
	ds_write_b16 v150, v137
	s_waitcnt lgkmcnt(0)
	s_barrier
	ds_read_b128 v[156:159], v147
	ds_read_b32 v137, v134 offset:64
	v_add_f32_e32 v135, v135, v136
	s_waitcnt lgkmcnt(1)
	v_smfmac_f32_16x16x64_f16 v[130:133], v[156:159], v[248:255], v191
	s_nop 7
	v_cndmask_b32_e64 v156, v130, v131, s[0:1]
	v_exp_f32_e64 v158, -|v156|
	v_max_f32 v159, 0, v156
	v_add_f32 v158, 1.0, v158
	v_log_f32 v158, v158
	s_nop 0
	v_fma_mixlo_f16 v157, v158, 1.0, v159
	ds_write_b16 v148, v157
	v_mov_b32_e32 v192, v106
	v_mov_b32_e32 v193, v110
	v_mul_f32 v136, -2.0, v137
	s_nop 6
	ds_read_b128 v[208:211], v139
	s_waitcnt lgkmcnt(1)
	s_barrier
	ds_read_b128 v[212:215], v140
	s_waitcnt lgkmcnt(1)
	v_smfmac_f32_16x16x64_f16 v[192:195], v[208:211], v[6:13], v191
	ds_read_b128 v[216:219], v141
	s_waitcnt lgkmcnt(1)
	v_smfmac_f32_16x16x64_f16 v[192:195], v[212:215], v[14:21], v191
	ds_read_b128 v[220:223], v142
	s_waitcnt lgkmcnt(1)
	v_smfmac_f32_16x16x64_f16 v[192:195], v[216:219], v[26:33], v191
	s_waitcnt lgkmcnt(0)
	v_smfmac_f32_16x16x64_f16 v[192:195], v[220:223], v[34:41], v191
	s_nop 7
	v_cndmask_b32_e64 v156, v192, v193, s[0:1]
	v_exp_f32_e64 v158, -|v156|
	v_max_f32 v159, 0, v156
	v_add_f32 v158, 1.0, v158
	v_log_f32 v158, v158
	s_nop 0
	v_fma_mixlo_f16 v157, v158, 1.0, v159
	ds_write_b16 v149, v157
	v_mov_b32_e32 v200, v114
	v_mov_b32_e32 v201, v118
	v_mov_b32_e32 v204, v122
	v_mov_b32_e32 v205, v126
	s_nop 2
	ds_read_b128 v[208:211], v143
	s_waitcnt lgkmcnt(1)
	s_barrier
	ds_read_b128 v[212:215], v144
	s_waitcnt lgkmcnt(1)
	v_smfmac_f32_16x16x64_f16 v[200:203], v[208:211], v[42:49], v191
	ds_read_b128 v[216:219], v145
	v_smfmac_f32_16x16x64_f16 v[204:207], v[208:211], v[74:81], v191
	ds_read_b128 v[220:223], v146
	s_waitcnt lgkmcnt(2)
	v_smfmac_f32_16x16x64_f16 v[200:203], v[212:215], v[50:57], v191
	v_smfmac_f32_16x16x64_f16 v[204:207], v[212:215], v[82:89], v191
	s_waitcnt lgkmcnt(1)
	v_smfmac_f32_16x16x64_f16 v[200:203], v[216:219], v[58:65], v191
	v_smfmac_f32_16x16x64_f16 v[204:207], v[216:219], v[90:97], v191
	s_waitcnt lgkmcnt(0)
	v_smfmac_f32_16x16x64_f16 v[200:203], v[220:223], v[66:73], v191
	v_smfmac_f32_16x16x64_f16 v[204:207], v[220:223], v[98:105], v191
	s_nop 6
	v_cndmask_b32_e64 v172, v201, v200, s[6:7]
	v_cndmask_b32_e64 v172, v172, v204, s[0:1]
	v_cndmask_b32_e64 v172, v172, v205, s[4:5]
	v_exp_f32_e32 v172, v172
	s_nop 0
	v_add_f32_e32 v172, 1.0, v172
	v_rcp_f32_e32 v172, v172
	s_nop 0
	v_fmac_f32_e32 v137, v172, v136
	s_nop 1
	v_add_f32_dpp v136, v137, v137 quad_perm:[1,0,3,2] row_mask:0xf bank_mask:0xf bound_ctrl:1
	s_nop 1
	v_add_f32_dpp v136, v136, v136 quad_perm:[2,3,0,1] row_mask:0xf bank_mask:0xf bound_ctrl:1
	s_nop 1
	v_add_f32_dpp v136, v136, v136 row_half_mirror row_mask:0xf bank_mask:0xf bound_ctrl:1
	v_cvt_f16_f32_e32 v137, v136
	ds_write_b16 v150, v137
	s_waitcnt lgkmcnt(0)
	s_barrier
	ds_read_b128 v[156:159], v147
	ds_read_b32 v137, v134 offset:96
	v_add_f32_e32 v135, v135, v136
	s_waitcnt lgkmcnt(1)
	v_smfmac_f32_16x16x64_f16 v[130:133], v[156:159], v[248:255], v191
	s_nop 7
	v_cndmask_b32_e64 v156, v130, v131, s[0:1]
	v_exp_f32_e64 v158, -|v156|
	v_max_f32 v159, 0, v156
	v_add_f32 v158, 1.0, v158
	v_log_f32 v158, v158
	s_nop 0
	v_fma_mixlo_f16 v157, v158, 1.0, v159
	ds_write_b16 v148, v157
	v_mov_b32_e32 v192, v106
	v_mov_b32_e32 v193, v110
	v_mul_f32 v136, -2.0, v137
	s_nop 6
	ds_read_b128 v[208:211], v139
	s_waitcnt lgkmcnt(1)
	s_barrier
	ds_read_b128 v[212:215], v140
	s_waitcnt lgkmcnt(1)
	v_smfmac_f32_16x16x64_f16 v[192:195], v[208:211], v[6:13], v191
	ds_read_b128 v[216:219], v141
	s_waitcnt lgkmcnt(1)
	v_smfmac_f32_16x16x64_f16 v[192:195], v[212:215], v[14:21], v191
	ds_read_b128 v[220:223], v142
	s_waitcnt lgkmcnt(1)
	v_smfmac_f32_16x16x64_f16 v[192:195], v[216:219], v[26:33], v191
	s_waitcnt lgkmcnt(0)
	v_smfmac_f32_16x16x64_f16 v[192:195], v[220:223], v[34:41], v191
	s_nop 7
	v_cndmask_b32_e64 v156, v192, v193, s[0:1]
	v_exp_f32_e64 v158, -|v156|
	v_max_f32 v159, 0, v156
	v_add_f32 v158, 1.0, v158
	v_log_f32 v158, v158
	s_nop 0
	v_fma_mixlo_f16 v157, v158, 1.0, v159
	ds_write_b16 v149, v157
	v_mov_b32_e32 v200, v114
	v_mov_b32_e32 v201, v118
	v_mov_b32_e32 v204, v122
	v_mov_b32_e32 v205, v126
	s_nop 2
	ds_read_b128 v[208:211], v143
	s_waitcnt lgkmcnt(1)
	s_barrier
	ds_read_b128 v[212:215], v144
	s_waitcnt lgkmcnt(1)
	v_smfmac_f32_16x16x64_f16 v[200:203], v[208:211], v[42:49], v191
	ds_read_b128 v[216:219], v145
	v_smfmac_f32_16x16x64_f16 v[204:207], v[208:211], v[74:81], v191
	ds_read_b128 v[220:223], v146
	s_waitcnt lgkmcnt(2)
	v_smfmac_f32_16x16x64_f16 v[200:203], v[212:215], v[50:57], v191
	v_smfmac_f32_16x16x64_f16 v[204:207], v[212:215], v[82:89], v191
	s_waitcnt lgkmcnt(1)
	v_smfmac_f32_16x16x64_f16 v[200:203], v[216:219], v[58:65], v191
	v_smfmac_f32_16x16x64_f16 v[204:207], v[216:219], v[90:97], v191
	s_waitcnt lgkmcnt(0)
	v_smfmac_f32_16x16x64_f16 v[200:203], v[220:223], v[66:73], v191
	v_smfmac_f32_16x16x64_f16 v[204:207], v[220:223], v[98:105], v191
	s_nop 6
	v_cndmask_b32_e64 v172, v201, v200, s[6:7]
	v_cndmask_b32_e64 v172, v172, v204, s[0:1]
	v_cndmask_b32_e64 v172, v172, v205, s[4:5]
	v_exp_f32_e32 v172, v172
	s_nop 0
	v_add_f32_e32 v172, 1.0, v172
	v_rcp_f32_e32 v172, v172
	s_nop 0
	v_fmac_f32_e32 v137, v172, v136
	s_nop 1
	v_add_f32_dpp v136, v137, v137 quad_perm:[1,0,3,2] row_mask:0xf bank_mask:0xf bound_ctrl:1
	s_nop 1
	v_add_f32_dpp v136, v136, v136 quad_perm:[2,3,0,1] row_mask:0xf bank_mask:0xf bound_ctrl:1
	s_nop 1
	v_add_f32_dpp v136, v136, v136 row_half_mirror row_mask:0xf bank_mask:0xf bound_ctrl:1
	v_cvt_f16_f32_e32 v137, v136
	ds_write_b16 v150, v137
	s_waitcnt lgkmcnt(0)
	s_barrier
	ds_read_b128 v[156:159], v147
	ds_read_b32 v137, v134 offset:128
	v_add_f32_e32 v135, v135, v136
	s_waitcnt lgkmcnt(1)
	v_smfmac_f32_16x16x64_f16 v[130:133], v[156:159], v[248:255], v191
	s_nop 7
	v_cndmask_b32_e64 v156, v130, v131, s[0:1]
	v_exp_f32_e64 v158, -|v156|
	v_max_f32 v159, 0, v156
	v_add_f32 v158, 1.0, v158
	v_log_f32 v158, v158
	s_nop 0
	v_fma_mixlo_f16 v157, v158, 1.0, v159
	ds_write_b16 v148, v157
	v_mov_b32_e32 v192, v106
	v_mov_b32_e32 v193, v110
	v_mul_f32 v136, -2.0, v137
	s_nop 6
	ds_read_b128 v[208:211], v139
	s_waitcnt lgkmcnt(1)
	s_barrier
	ds_read_b128 v[212:215], v140
	s_waitcnt lgkmcnt(1)
	v_smfmac_f32_16x16x64_f16 v[192:195], v[208:211], v[6:13], v191
	ds_read_b128 v[216:219], v141
	s_waitcnt lgkmcnt(1)
	v_smfmac_f32_16x16x64_f16 v[192:195], v[212:215], v[14:21], v191
	ds_read_b128 v[220:223], v142
	s_waitcnt lgkmcnt(1)
	v_smfmac_f32_16x16x64_f16 v[192:195], v[216:219], v[26:33], v191
	s_waitcnt lgkmcnt(0)
	v_smfmac_f32_16x16x64_f16 v[192:195], v[220:223], v[34:41], v191
	s_nop 7
	v_cndmask_b32_e64 v156, v192, v193, s[0:1]
	v_exp_f32_e64 v158, -|v156|
	v_max_f32 v159, 0, v156
	v_add_f32 v158, 1.0, v158
	v_log_f32 v158, v158
	s_nop 0
	v_fma_mixlo_f16 v157, v158, 1.0, v159
	ds_write_b16 v149, v157
	v_mov_b32_e32 v200, v114
	v_mov_b32_e32 v201, v118
	v_mov_b32_e32 v204, v122
	v_mov_b32_e32 v205, v126
	s_nop 2
	ds_read_b128 v[208:211], v143
	s_waitcnt lgkmcnt(1)
	s_barrier
	ds_read_b128 v[212:215], v144
	s_waitcnt lgkmcnt(1)
	v_smfmac_f32_16x16x64_f16 v[200:203], v[208:211], v[42:49], v191
	ds_read_b128 v[216:219], v145
	v_smfmac_f32_16x16x64_f16 v[204:207], v[208:211], v[74:81], v191
	ds_read_b128 v[220:223], v146
	s_waitcnt lgkmcnt(2)
	v_smfmac_f32_16x16x64_f16 v[200:203], v[212:215], v[50:57], v191
	v_smfmac_f32_16x16x64_f16 v[204:207], v[212:215], v[82:89], v191
	s_waitcnt lgkmcnt(1)
	v_smfmac_f32_16x16x64_f16 v[200:203], v[216:219], v[58:65], v191
	v_smfmac_f32_16x16x64_f16 v[204:207], v[216:219], v[90:97], v191
	s_waitcnt lgkmcnt(0)
	v_smfmac_f32_16x16x64_f16 v[200:203], v[220:223], v[66:73], v191
	v_smfmac_f32_16x16x64_f16 v[204:207], v[220:223], v[98:105], v191
	s_nop 6
	v_cndmask_b32_e64 v172, v201, v200, s[6:7]
	v_cndmask_b32_e64 v172, v172, v204, s[0:1]
	v_cndmask_b32_e64 v172, v172, v205, s[4:5]
	v_exp_f32_e32 v172, v172
	s_nop 0
	v_add_f32_e32 v172, 1.0, v172
	v_rcp_f32_e32 v172, v172
	s_nop 0
	v_fmac_f32_e32 v137, v172, v136
	s_nop 1
	v_add_f32_dpp v136, v137, v137 quad_perm:[1,0,3,2] row_mask:0xf bank_mask:0xf bound_ctrl:1
	s_nop 1
	v_add_f32_dpp v136, v136, v136 quad_perm:[2,3,0,1] row_mask:0xf bank_mask:0xf bound_ctrl:1
	s_nop 1
	v_add_f32_dpp v136, v136, v136 row_half_mirror row_mask:0xf bank_mask:0xf bound_ctrl:1
	v_cvt_f16_f32_e32 v137, v136
	ds_write_b16 v150, v137
	s_waitcnt lgkmcnt(0)
	s_barrier
	ds_read_b128 v[156:159], v147
	ds_read_b32 v137, v134 offset:160
	v_add_f32_e32 v135, v135, v136
	s_waitcnt lgkmcnt(1)
	v_smfmac_f32_16x16x64_f16 v[130:133], v[156:159], v[248:255], v191
	s_nop 7
	v_cndmask_b32_e64 v156, v130, v131, s[0:1]
	v_exp_f32_e64 v158, -|v156|
	v_max_f32 v159, 0, v156
	v_add_f32 v158, 1.0, v158
	v_log_f32 v158, v158
	s_nop 0
	v_fma_mixlo_f16 v157, v158, 1.0, v159
	ds_write_b16 v148, v157
	v_mov_b32_e32 v192, v106
	v_mov_b32_e32 v193, v110
	v_mul_f32 v136, -2.0, v137
	s_nop 6
	ds_read_b128 v[208:211], v139
	s_waitcnt lgkmcnt(1)
	s_barrier
	ds_read_b128 v[212:215], v140
	s_waitcnt lgkmcnt(1)
	v_smfmac_f32_16x16x64_f16 v[192:195], v[208:211], v[6:13], v191
	ds_read_b128 v[216:219], v141
	s_waitcnt lgkmcnt(1)
	v_smfmac_f32_16x16x64_f16 v[192:195], v[212:215], v[14:21], v191
	ds_read_b128 v[220:223], v142
	s_waitcnt lgkmcnt(1)
	v_smfmac_f32_16x16x64_f16 v[192:195], v[216:219], v[26:33], v191
	s_waitcnt lgkmcnt(0)
	v_smfmac_f32_16x16x64_f16 v[192:195], v[220:223], v[34:41], v191
	s_nop 7
	v_cndmask_b32_e64 v156, v192, v193, s[0:1]
	v_exp_f32_e64 v158, -|v156|
	v_max_f32 v159, 0, v156
	v_add_f32 v158, 1.0, v158
	v_log_f32 v158, v158
	s_nop 0
	v_fma_mixlo_f16 v157, v158, 1.0, v159
	ds_write_b16 v149, v157
	v_mov_b32_e32 v200, v114
	v_mov_b32_e32 v201, v118
	v_mov_b32_e32 v204, v122
	v_mov_b32_e32 v205, v126
	s_nop 2
	ds_read_b128 v[208:211], v143
	s_waitcnt lgkmcnt(1)
	s_barrier
	ds_read_b128 v[212:215], v144
	s_waitcnt lgkmcnt(1)
	v_smfmac_f32_16x16x64_f16 v[200:203], v[208:211], v[42:49], v191
	ds_read_b128 v[216:219], v145
	v_smfmac_f32_16x16x64_f16 v[204:207], v[208:211], v[74:81], v191
	ds_read_b128 v[220:223], v146
	s_waitcnt lgkmcnt(2)
	v_smfmac_f32_16x16x64_f16 v[200:203], v[212:215], v[50:57], v191
	v_smfmac_f32_16x16x64_f16 v[204:207], v[212:215], v[82:89], v191
	s_waitcnt lgkmcnt(1)
	v_smfmac_f32_16x16x64_f16 v[200:203], v[216:219], v[58:65], v191
	v_smfmac_f32_16x16x64_f16 v[204:207], v[216:219], v[90:97], v191
	s_waitcnt lgkmcnt(0)
	v_smfmac_f32_16x16x64_f16 v[200:203], v[220:223], v[66:73], v191
	v_smfmac_f32_16x16x64_f16 v[204:207], v[220:223], v[98:105], v191
	s_nop 6
	v_cndmask_b32_e64 v172, v201, v200, s[6:7]
	v_cndmask_b32_e64 v172, v172, v204, s[0:1]
	v_cndmask_b32_e64 v172, v172, v205, s[4:5]
	v_exp_f32_e32 v172, v172
	s_nop 0
	v_add_f32_e32 v172, 1.0, v172
	v_rcp_f32_e32 v172, v172
	s_nop 0
	v_fmac_f32_e32 v137, v172, v136
	s_nop 1
	v_add_f32_dpp v136, v137, v137 quad_perm:[1,0,3,2] row_mask:0xf bank_mask:0xf bound_ctrl:1
	s_nop 1
	v_add_f32_dpp v136, v136, v136 quad_perm:[2,3,0,1] row_mask:0xf bank_mask:0xf bound_ctrl:1
	s_nop 1
	v_add_f32_dpp v136, v136, v136 row_half_mirror row_mask:0xf bank_mask:0xf bound_ctrl:1
	v_cvt_f16_f32_e32 v137, v136
	ds_write_b16 v150, v137
	s_waitcnt lgkmcnt(0)
	s_barrier
	ds_read_b128 v[156:159], v147
	ds_read_b32 v137, v134 offset:192
	v_add_f32_e32 v135, v135, v136
	s_waitcnt lgkmcnt(1)
	v_smfmac_f32_16x16x64_f16 v[130:133], v[156:159], v[248:255], v191
	s_nop 7
	v_cndmask_b32_e64 v152, v130, v131, s[0:1]
	v_exp_f32_e64 v158, -|v152|
	v_max_f32 v159, 0, v152
	v_add_f32 v158, 1.0, v158
	v_log_f32 v158, v158
	s_nop 0
	v_fma_mixlo_f16 v153, v158, 1.0, v159
	ds_write_b16 v148, v153
	v_mov_b32_e32 v192, v106
	v_mov_b32_e32 v193, v110
	v_mul_f32 v136, -2.0, v137
	s_nop 6
	ds_read_b128 v[208:211], v139
	s_waitcnt lgkmcnt(1)
	s_barrier
	ds_read_b128 v[212:215], v140
	s_waitcnt lgkmcnt(1)
	v_smfmac_f32_16x16x64_f16 v[192:195], v[208:211], v[6:13], v191
	ds_read_b128 v[216:219], v141
	s_waitcnt lgkmcnt(1)
	v_smfmac_f32_16x16x64_f16 v[192:195], v[212:215], v[14:21], v191
	ds_read_b128 v[220:223], v142
	s_waitcnt lgkmcnt(1)
	v_smfmac_f32_16x16x64_f16 v[192:195], v[216:219], v[26:33], v191
	s_waitcnt lgkmcnt(0)
	v_smfmac_f32_16x16x64_f16 v[192:195], v[220:223], v[34:41], v191
	s_nop 7
	v_cndmask_b32_e64 v152, v192, v193, s[0:1]
	v_exp_f32_e64 v158, -|v152|
	v_max_f32 v159, 0, v152
	v_add_f32 v158, 1.0, v158
	v_log_f32 v158, v158
	s_nop 0
	v_fma_mixlo_f16 v153, v158, 1.0, v159
	ds_write_b16 v149, v153
	v_mov_b32_e32 v200, v114
	v_mov_b32_e32 v201, v118
	v_mov_b32_e32 v204, v122
	v_mov_b32_e32 v205, v126
	s_nop 2
	ds_read_b128 v[208:211], v143
	s_waitcnt lgkmcnt(1)
	s_barrier
	ds_read_b128 v[212:215], v144
	s_waitcnt lgkmcnt(1)
	v_smfmac_f32_16x16x64_f16 v[200:203], v[208:211], v[42:49], v191
	ds_read_b128 v[216:219], v145
	v_smfmac_f32_16x16x64_f16 v[204:207], v[208:211], v[74:81], v191
	ds_read_b128 v[220:223], v146
	s_waitcnt lgkmcnt(2)
	v_smfmac_f32_16x16x64_f16 v[200:203], v[212:215], v[50:57], v191
	v_smfmac_f32_16x16x64_f16 v[204:207], v[212:215], v[82:89], v191
	s_waitcnt lgkmcnt(1)
	v_smfmac_f32_16x16x64_f16 v[200:203], v[216:219], v[58:65], v191
	v_smfmac_f32_16x16x64_f16 v[204:207], v[216:219], v[90:97], v191
	s_waitcnt lgkmcnt(0)
	v_smfmac_f32_16x16x64_f16 v[200:203], v[220:223], v[66:73], v191
	v_smfmac_f32_16x16x64_f16 v[204:207], v[220:223], v[98:105], v191
	s_nop 6
	v_cndmask_b32_e64 v152, v201, v200, s[6:7]
	v_cndmask_b32_e64 v152, v152, v204, s[0:1]
	v_cndmask_b32_e64 v152, v152, v205, s[4:5]
	v_exp_f32_e32 v152, v152
	s_nop 0
	v_add_f32_e32 v152, 1.0, v152
	v_rcp_f32_e32 v152, v152
	s_nop 0
	v_fmac_f32_e32 v137, v152, v136
	s_nop 1
	v_add_f32_dpp v136, v137, v137 quad_perm:[1,0,3,2] row_mask:0xf bank_mask:0xf bound_ctrl:1
	s_nop 1
	v_add_f32_dpp v136, v136, v136 quad_perm:[2,3,0,1] row_mask:0xf bank_mask:0xf bound_ctrl:1
	s_nop 1
	v_add_f32_dpp v136, v136, v136 row_half_mirror row_mask:0xf bank_mask:0xf bound_ctrl:1
	v_cvt_f16_f32_e32 v137, v136
	ds_write_b16 v150, v137
	s_waitcnt lgkmcnt(0)
	s_barrier
	ds_read_b128 v[158:161], v147
	v_add_f32_e32 v152, v135, v136
	ds_read_b32 v153, v134 offset:224
	s_addk_i32 s3, 0x100
	s_cmpk_eq_u32 s3, 0xfa20
	s_waitcnt lgkmcnt(1)
	v_smfmac_f32_16x16x64_f16 v[130:133], v[158:161], v[248:255], v191
	s_nop 7
	v_cndmask_b32_e64 v154, v130, v131, s[0:1]
	s_cbranch_scc0 .LBB0_21
	s_and_saveexec_b64 s[0:1], vcc
	ds_write_b32 v1, v152
	s_or_b64 exec, exec, s[0:1]
	v_cmp_gt_u32_e32 vcc, 10, v0
	s_waitcnt lgkmcnt(0)
	s_barrier
	s_and_saveexec_b64 s[0:1], vcc
	s_cbranch_execz .LBB0_28
	v_lshlrev_b32_e32 v1, 2, v0
	global_load_dword v1, v1, s[12:13]
	v_mov_b32_e32 v139, 0
	v_lshl_add_u64 v[2:3], s[10:11], 0, v[138:139]
	v_lshl_add_u64 v[2:3], v[2:3], 0, 28
	s_mov_b32 s0, 0
